# SB and MEM attention tile loops: next-tile K/V global loads issued after the Q re-read sequence so the counted vmcnt waits of QK no longer wait for them
# baseline (speedup 1.0000x reference)
.LBB0_799:
	v_add_u32_e32 v1, v185, v155
	s_waitcnt lgkmcnt(0)
	s_barrier
	ds_read_b128 v[72:75], v1
	ds_read_b128 v[76:79], v1 offset:8192
	s_waitcnt vmcnt(7) lgkmcnt(1)
	v_mfma_f32_32x32x16_bf16 v[84:99], v[72:75], v[68:71], 0
	v_add_u32_e32 v1, v185, v157
	ds_read_b128 v[200:203], v1
	ds_read_b128 v[204:207], v1 offset:8192
	v_add_u32_e32 v1, v185, v159
	s_waitcnt lgkmcnt(2)
	v_mfma_f32_32x32x16_bf16 v[68:83], v[76:79], v[68:71], 0
	s_waitcnt vmcnt(6) lgkmcnt(1)
	v_mfma_f32_32x32x16_bf16 v[84:99], v[200:203], v[140:143], v[84:99]
	s_waitcnt lgkmcnt(0)
	v_mfma_f32_32x32x16_bf16 v[68:83], v[204:207], v[140:143], v[68:83]
	ds_read_b128 v[140:143], v1
	ds_read_b128 v[200:203], v1 offset:8192
	v_add_u32_e32 v1, v185, v161
	s_waitcnt vmcnt(5) lgkmcnt(1)
	v_mfma_f32_32x32x16_bf16 v[84:99], v[140:143], v[136:139], v[84:99]
	s_waitcnt lgkmcnt(0)
	v_mfma_f32_32x32x16_bf16 v[68:83], v[200:203], v[136:139], v[68:83]
	ds_read_b128 v[136:139], v1
	ds_read_b128 v[140:143], v1 offset:8192
	v_add_u32_e32 v1, v185, v163
	s_waitcnt vmcnt(4) lgkmcnt(1)
	v_mfma_f32_32x32x16_bf16 v[84:99], v[136:139], v[132:135], v[84:99]
	s_waitcnt lgkmcnt(0)
	v_mfma_f32_32x32x16_bf16 v[68:83], v[140:143], v[132:135], v[68:83]
	ds_read_b128 v[132:135], v1
	ds_read_b128 v[136:139], v1 offset:8192
	v_add_u32_e32 v1, v185, v165
	s_waitcnt vmcnt(3) lgkmcnt(1)
	v_mfma_f32_32x32x16_bf16 v[84:99], v[132:135], v[128:131], v[84:99]
	s_waitcnt lgkmcnt(0)
	v_mfma_f32_32x32x16_bf16 v[68:83], v[136:139], v[128:131], v[68:83]
	ds_read_b128 v[128:131], v1
	ds_read_b128 v[132:135], v1 offset:8192
	v_add_u32_e32 v1, v185, v167
	s_waitcnt vmcnt(2) lgkmcnt(1)
	v_mfma_f32_32x32x16_bf16 v[84:99], v[128:131], v[124:127], v[84:99]
	s_waitcnt lgkmcnt(0)
	v_mfma_f32_32x32x16_bf16 v[68:83], v[132:135], v[124:127], v[68:83]
	ds_read_b128 v[124:127], v1
	ds_read_b128 v[128:131], v1 offset:8192
	v_add_u32_e32 v1, v185, v169
	s_waitcnt vmcnt(1) lgkmcnt(1)
	v_mfma_f32_32x32x16_bf16 v[84:99], v[124:127], v[120:123], v[84:99]
	s_waitcnt lgkmcnt(0)
	v_mfma_f32_32x32x16_bf16 v[68:83], v[128:131], v[120:123], v[68:83]
	ds_read_b128 v[120:123], v1
	ds_read_b128 v[124:127], v1 offset:8192
	s_waitcnt vmcnt(0) lgkmcnt(1)
	v_mfma_f32_32x32x16_bf16 v[84:99], v[120:123], v[116:119], v[84:99]
	s_cmp_ge_u32 s2, s88
	s_cbranch_scc1 .Lsbkv_skip
	v_add_u32_e32 v1, s96, v197
	v_add_u32_e32 v2, 0x1f80, v1
	v_mad_i64_i32 v[128:129], s[0:1], v2, s33, v[190:191]
	v_add_u32_e32 v1, 0x1fa0, v1
	v_mad_i64_i32 v[130:131], s[0:1], v1, s33, v[190:191]
	global_load_dwordx4 v[100:103], v[128:129], off
	global_load_dwordx4 v[104:107], v[130:131], off
	v_mad_i64_i32 v[128:129], s[0:1], v2, s33, v[188:189]
	v_mad_i64_i32 v[130:131], s[0:1], v1, s33, v[188:189]
	global_load_dwordx4 v[108:111], v[128:129], off
	global_load_dwordx4 v[112:115], v[130:131], off
.Lsbkv_skip:
	v_add_u32_e32 v122, s96, v177
	v_add_u32_e32 v129, 0x1fca, v122
	v_add_u32_e32 v1, 0x1fc0, v122
	v_cmp_lt_i32_e64 s[18:19], v129, v176
	v_cmp_lt_i32_e32 vcc, v1, v176
	v_add_u32_e32 v131, 0x1fcb, v122
	v_cmp_lt_i32_e64 s[20:21], v131, v176
	s_nop 4
	v_max_f32_e32 v2, v84, v84
	v_max_f32_e32 v84, v85, v85
	v_min_f32_e32 v2, 0x42a00000, v2
	v_min_f32_e32 v84, 0x42a00000, v84
	v_max_f32_e32 v85, v86, v86
	s_waitcnt lgkmcnt(0)
	v_mfma_f32_32x32x16_bf16 v[68:83], v[124:127], v[116:119], v[68:83]
	v_exp_f32_e32 v116, v2
	v_exp_f32_e32 v118, v84
	v_min_f32_e32 v85, 0x42a00000, v85
	v_max_f32_e32 v87, v87, v87
	v_exp_f32_e32 v86, v85
	v_min_f32_e32 v87, 0x42a00000, v87
	v_exp_f32_e32 v87, v87
	v_max_f32_e32 v88, v88, v88
	v_max_f32_e32 v89, v89, v89
	v_add_f32_e32 v2, 1.0, v116
	v_add_f32_e32 v84, 1.0, v118
	v_min_f32_e32 v88, 0x42a00000, v88
	v_min_f32_e32 v89, 0x42a00000, v89
	v_max_f32_e32 v90, v90, v90
	v_rcp_f32_e32 v117, v2
	v_rcp_f32_e32 v119, v84
	v_add_f32_e32 v85, 1.0, v86
	v_exp_f32_e32 v88, v88
	v_exp_f32_e32 v89, v89
	v_min_f32_e32 v90, 0x42a00000, v90
	v_max_f32_e32 v91, v91, v91
	v_rcp_f32_e32 v120, v85
	v_add_f32_e32 v121, 1.0, v87
	v_exp_f32_e32 v127, v90
	v_min_f32_e32 v91, 0x42a00000, v91
	v_add_u32_e32 v2, 0x1fc1, v122
	v_rcp_f32_e32 v121, v121
	v_exp_f32_e32 v129, v91
	v_cmp_lt_i32_e64 s[8:9], v2, v176
	v_add_u32_e32 v84, 0x1fc2, v122
	v_max_f32_e32 v92, v92, v92
	v_max_f32_e32 v93, v93, v93
	v_cndmask_b32_e32 v1, 1.0, v117, vcc
	v_cndmask_b32_e64 v2, 1.0, v119, s[8:9]
	v_cmp_lt_i32_e64 s[10:11], v84, v176
	v_add_u32_e32 v85, 0x1fc3, v122
	v_add_f32_e32 v124, 1.0, v88
	v_add_f32_e32 v126, 1.0, v89
	v_min_f32_e32 v92, 0x42a00000, v92
	v_min_f32_e32 v93, 0x42a00000, v93
	v_max_f32_e32 v94, v94, v94
	v_mul_f32_e32 v1, v1, v2
	v_cndmask_b32_e64 v84, 1.0, v120, s[10:11]
	v_cmp_lt_i32_e64 s[12:13], v85, v176
	v_rcp_f32_e32 v124, v124
	v_rcp_f32_e32 v126, v126
	v_add_f32_e32 v90, 1.0, v127
	v_exp_f32_e32 v131, v92
	v_exp_f32_e32 v134, v93
	v_min_f32_e32 v94, 0x42a00000, v94
	v_max_f32_e32 v95, v95, v95
	v_mul_f32_e32 v1, v84, v1
	v_cndmask_b32_e64 v85, 1.0, v121, s[12:13]
	v_rcp_f32_e32 v128, v90
	v_add_f32_e32 v91, 1.0, v129
	v_exp_f32_e32 v136, v94
	v_min_f32_e32 v95, 0x42a00000, v95
	v_mul_f32_e32 v123, v85, v1
	v_add_u32_e32 v1, 0x1fc8, v122
	v_add_u32_e32 v125, 0x1fc9, v122
	v_rcp_f32_e32 v130, v91
	v_exp_f32_e32 v95, v95
	v_cmp_lt_i32_e64 s[14:15], v1, v176
	v_cmp_lt_i32_e64 s[16:17], v125, v176
	v_max_f32_e32 v96, v96, v96
	v_max_f32_e32 v97, v97, v97
	v_cndmask_b32_e64 v1, 1.0, v124, s[14:15]
	v_cndmask_b32_e64 v125, 1.0, v126, s[16:17]
	v_add_f32_e32 v92, 1.0, v131
	v_add_f32_e32 v93, 1.0, v134
	v_min_f32_e32 v96, 0x42a00000, v96
	v_min_f32_e32 v97, 0x42a00000, v97
	v_max_f32_e32 v98, v98, v98
	v_mul_f32_e32 v1, v1, v125
	v_cndmask_b32_e64 v90, 1.0, v128, s[18:19]
	v_rcp_f32_e32 v133, v92
	v_rcp_f32_e32 v135, v93
	v_add_f32_e32 v94, 1.0, v136
	v_exp_f32_e32 v139, v96
	v_exp_f32_e32 v142, v97
	v_min_f32_e32 v98, 0x42a00000, v98
	v_max_f32_e32 v99, v99, v99
	v_mul_f32_e32 v1, v90, v1
	v_cndmask_b32_e64 v91, 1.0, v130, s[20:21]
	v_rcp_f32_e32 v137, v94
	v_add_f32_e32 v138, 1.0, v95
	v_exp_f32_e32 v199, v98
	v_min_f32_e32 v99, 0x42a00000, v99
	v_mul_f32_e32 v132, v91, v1
	v_add_u32_e32 v1, 0x1fd0, v122
	v_add_u32_e32 v92, 0x1fd1, v122
	v_rcp_f32_e32 v138, v138
	v_exp_f32_e32 v99, v99
	v_cmp_lt_i32_e64 s[22:23], v1, v176
	v_cmp_lt_i32_e64 s[24:25], v92, v176
	v_add_u32_e32 v93, 0x1fd2, v122
	v_max_f32_e32 v68, v68, v68
	v_max_f32_e32 v69, v69, v69
	v_cndmask_b32_e64 v1, 1.0, v133, s[22:23]
	v_cndmask_b32_e64 v92, 1.0, v135, s[24:25]
	v_cmp_lt_i32_e64 s[26:27], v93, v176
	v_add_u32_e32 v94, 0x1fd3, v122
	v_add_f32_e32 v96, 1.0, v139
	v_add_f32_e32 v97, 1.0, v142
	v_min_f32_e32 v68, 0x42a00000, v68
	v_min_f32_e32 v69, 0x42a00000, v69
	v_max_f32_e32 v70, v70, v70
	v_mul_f32_e32 v1, v1, v92
	v_cndmask_b32_e64 v93, 1.0, v137, s[26:27]
	v_cmp_lt_i32_e64 s[28:29], v94, v176
	v_rcp_f32_e32 v140, v96
	v_rcp_f32_e32 v143, v97
	v_add_f32_e32 v98, 1.0, v199
	v_exp_f32_e32 v202, v68
	v_exp_f32_e32 v204, v69
	v_min_f32_e32 v70, 0x42a00000, v70
	v_max_f32_e32 v71, v71, v71
	v_mul_f32_e32 v1, v93, v1
	v_cndmask_b32_e64 v94, 1.0, v138, s[28:29]
	v_rcp_f32_e32 v200, v98
	v_add_f32_e32 v201, 1.0, v99
	v_exp_f32_e32 v207, v70
	v_min_f32_e32 v71, 0x42a00000, v71
	v_mul_f32_e32 v141, v94, v1
	v_add_u32_e32 v1, 0x1fd8, v122
	v_add_u32_e32 v96, 0x1fd9, v122
	v_rcp_f32_e32 v201, v201
	v_exp_f32_e32 v71, v71
	v_cmp_lt_i32_e64 s[30:31], v1, v176
	v_cmp_lt_i32_e64 s[34:35], v96, v176
	v_add_u32_e32 v97, 0x1fda, v122
	v_max_f32_e32 v72, v72, v72
	v_max_f32_e32 v73, v73, v73
	v_cndmask_b32_e64 v1, 1.0, v140, s[30:31]
	v_cndmask_b32_e64 v96, 1.0, v143, s[34:35]
	v_cmp_lt_i32_e64 s[36:37], v97, v176
	v_add_u32_e32 v98, 0x1fdb, v122
	v_add_f32_e32 v68, 1.0, v202
	v_add_f32_e32 v69, 1.0, v204
	v_min_f32_e32 v72, 0x42a00000, v72
	v_min_f32_e32 v73, 0x42a00000, v73
	v_max_f32_e32 v74, v74, v74
	v_mul_f32_e32 v1, v1, v96
	v_cndmask_b32_e64 v97, 1.0, v200, s[36:37]
	v_cmp_lt_i32_e64 s[38:39], v98, v176
	v_rcp_f32_e32 v203, v68
	v_rcp_f32_e32 v206, v69
	v_add_f32_e32 v70, 1.0, v207
	v_exp_f32_e32 v72, v72
	v_add_u32_e32 v214, 0x1fe9, v122
	v_exp_f32_e32 v211, v73
	v_min_f32_e32 v74, 0x42a00000, v74
	v_max_f32_e32 v75, v75, v75
	v_mul_f32_e32 v1, v97, v1
	v_cndmask_b32_e64 v98, 1.0, v201, s[38:39]
	v_rcp_f32_e32 v208, v70
	v_add_f32_e32 v209, 1.0, v71
	v_cmp_lt_i32_e64 s[50:51], v214, v176
	v_exp_f32_e32 v214, v74
	v_min_f32_e32 v75, 0x42a00000, v75
	v_mul_f32_e32 v205, v98, v1
	v_add_u32_e32 v1, 0x1fe0, v122
	v_add_u32_e32 v68, 0x1fe1, v122
	v_rcp_f32_e32 v209, v209
	v_exp_f32_e32 v217, v75
	v_cmp_lt_i32_e64 s[40:41], v1, v176
	v_cmp_lt_i32_e64 s[42:43], v68, v176
	v_add_u32_e32 v69, 0x1fe2, v122
	v_max_f32_e32 v76, v76, v76
	v_max_f32_e32 v77, v77, v77
	v_cndmask_b32_e64 v1, 1.0, v203, s[40:41]
	v_cndmask_b32_e64 v68, 1.0, v206, s[42:43]
	v_cmp_lt_i32_e64 s[44:45], v69, v176
	v_add_u32_e32 v70, 0x1fe3, v122
	v_add_f32_e32 v210, 1.0, v72
	v_add_f32_e32 v73, 1.0, v211
	v_min_f32_e32 v76, 0x42a00000, v76
	v_min_f32_e32 v77, 0x42a00000, v77
	v_max_f32_e32 v78, v78, v78
	v_mul_f32_e32 v1, v1, v68
	v_cndmask_b32_e64 v69, 1.0, v208, s[44:45]
	v_cmp_lt_i32_e64 s[46:47], v70, v176
	v_rcp_f32_e32 v210, v210
	v_rcp_f32_e32 v212, v73
	v_add_f32_e32 v74, 1.0, v214
	v_exp_f32_e32 v219, v76
	v_exp_f32_e32 v221, v77
	v_min_f32_e32 v78, 0x42a00000, v78
	v_max_f32_e32 v79, v79, v79
	v_mul_f32_e32 v1, v69, v1
	v_cndmask_b32_e64 v70, 1.0, v209, s[46:47]
	v_rcp_f32_e32 v215, v74
	v_add_f32_e32 v75, 1.0, v217
	v_exp_f32_e32 v224, v78
	v_min_f32_e32 v79, 0x42a00000, v79
	v_mul_f32_e32 v213, v70, v1
	v_add_u32_e32 v1, 0x1fe8, v122
	v_rcp_f32_e32 v218, v75
	v_exp_f32_e32 v226, v79
	v_cmp_lt_i32_e64 s[48:49], v1, v176
	v_add_u32_e32 v216, 0x1fea, v122
	v_max_f32_e32 v80, v80, v80
	v_cndmask_b32_e64 v1, 1.0, v210, s[48:49]
	v_cndmask_b32_e64 v73, 1.0, v212, s[50:51]
	v_cmp_lt_i32_e64 s[52:53], v216, v176
	v_add_u32_e32 v216, 0x1feb, v122
	v_add_f32_e32 v76, 1.0, v219
	v_add_f32_e32 v77, 1.0, v221
	v_min_f32_e32 v80, 0x42a00000, v80
	v_mul_f32_e32 v1, v1, v73
	v_cndmask_b32_e64 v74, 1.0, v215, s[52:53]
	v_cmp_lt_i32_e64 s[54:55], v216, v176
	v_rcp_f32_e32 v220, v76
	v_rcp_f32_e32 v222, v77
	v_add_f32_e32 v78, 1.0, v224
	v_exp_f32_e32 v80, v80
	v_mul_f32_e32 v1, v74, v1
	v_cndmask_b32_e64 v75, 1.0, v218, s[54:55]
	v_rcp_f32_e32 v225, v78
	v_add_f32_e32 v79, 1.0, v226
	v_mul_f32_e32 v223, v75, v1
	v_add_u32_e32 v1, 0x1ff0, v122
	v_add_u32_e32 v76, 0x1ff1, v122
	v_rcp_f32_e32 v227, v79
	v_cmp_lt_i32_e64 s[56:57], v1, v176
	v_cmp_lt_i32_e64 s[58:59], v76, v176
	v_add_u32_e32 v76, 0x1ff2, v122
	v_max_f32_e32 v81, v81, v81
	v_cndmask_b32_e64 v1, 1.0, v220, s[56:57]
	v_cndmask_b32_e64 v77, 1.0, v222, s[58:59]
	v_cmp_lt_i32_e64 s[60:61], v76, v176
	v_add_u32_e32 v76, 0x1ff3, v122
	v_add_f32_e32 v216, 1.0, v80
	v_min_f32_e32 v81, 0x42a00000, v81
	v_max_f32_e32 v82, v82, v82
	v_mul_f32_e32 v1, v1, v77
	v_cndmask_b32_e64 v78, 1.0, v225, s[60:61]
	v_cmp_lt_i32_e64 s[62:63], v76, v176
	v_rcp_f32_e32 v228, v216
	v_add_u32_e32 v216, 0x1ff9, v122
	v_exp_f32_e32 v81, v81
	v_min_f32_e32 v82, 0x42a00000, v82
	v_max_f32_e32 v83, v83, v83
	v_mul_f32_e32 v1, v78, v1
	v_cndmask_b32_e64 v79, 1.0, v227, s[62:63]
	v_cmp_lt_i32_e64 s[66:67], v216, v176
	v_add_u32_e32 v216, 0x1ffa, v122
	v_exp_f32_e32 v82, v82
	v_min_f32_e32 v83, 0x42a00000, v83
	v_mul_f32_e32 v76, v79, v1
	v_add_u32_e32 v1, 0x1ff8, v122
	v_cmp_lt_i32_e64 s[68:69], v216, v176
	v_add_u32_e32 v216, 0x1ffb, v122
	v_exp_f32_e32 v122, v83
	v_add_f32_e32 v229, 1.0, v81
	v_rcp_f32_e32 v230, v229
	v_add_f32_e32 v231, 1.0, v82
	v_rcp_f32_e32 v232, v231
	v_add_f32_e32 v83, 1.0, v122
	v_rcp_f32_e32 v235, v83
	v_cmp_lt_i32_e64 s[64:65], v1, v176
	v_cndmask_b32_e64 v229, 1.0, v230, s[66:67]
	v_cndmask_b32_e64 v231, 1.0, v232, s[68:69]
	v_cndmask_b32_e64 v1, 1.0, v228, s[64:65]
	v_mul_f32_e32 v1, v1, v229
	v_cmp_lt_i32_e64 s[70:71], v216, v176
	v_mul_f32_e32 v1, v231, v1
	v_mov_b32_e32 v83, v123
	v_cndmask_b32_e64 v236, 1.0, v235, s[70:71]
	v_mul_f32_e32 v240, v236, v1
	v_mov_b32_e32 v233, v123
	v_mov_b32_e32 v234, v132
	v_mov_b32_e32 v237, v132
	v_mov_b32_e32 v238, v141
	v_mov_b32_e32 v239, v141
	v_mov_b32_e32 v241, v205
	v_mov_b32_e32 v242, v205
	v_mov_b32_e32 v243, v213
	v_mov_b32_e32 v244, v213
	v_mov_b32_e32 v245, v223
	v_mov_b32_e32 v246, v223
	v_mov_b32_e32 v247, v76
	v_mov_b32_e32 v248, v76
	v_mov_b32_e32 v249, v240
	v_mov_b32_e32 v250, v240
	v_permlane32_swap_b32_e32 v83, v233
	v_permlane32_swap_b32_e32 v234, v237
	v_permlane32_swap_b32_e32 v238, v239
	v_permlane32_swap_b32_e32 v241, v242
	v_permlane32_swap_b32_e32 v243, v244
	v_permlane32_swap_b32_e32 v245, v246
	v_permlane32_swap_b32_e32 v247, v248
	v_permlane32_swap_b32_e32 v249, v250
	s_and_saveexec_b64 s[0:1], s[6:7]
	v_mov_b32_e32 v1, s77
	ds_write_b32 v1, v3 offset:51712
	s_or_b64 exec, exec, s[0:1]
	v_cndmask_b32_e64 v83, v83, v233, s[4:5]
	v_cndmask_b32_e64 v233, v234, v237, s[4:5]
	v_cndmask_b32_e64 v234, v238, v239, s[4:5]
	v_cndmask_b32_e64 v237, v241, v242, s[4:5]
	v_cndmask_b32_e64 v238, v243, v244, s[4:5]
	v_cndmask_b32_e64 v241, v247, v248, s[4:5]
	v_cndmask_b32_e64 v243, v249, v250, s[4:5]
	v_cndmask_b32_e64 v239, v245, v246, s[4:5]
	v_mul_f32_e32 v242, v240, v243
	v_mul_f32_e32 v1, v76, v241
	v_mul_f32_e32 v240, v1, v242
	v_mul_f32_e32 v1, v223, v239
	v_mul_f32_e32 v223, v1, v240
	v_mul_f32_e32 v1, v213, v238
	v_mul_f32_e32 v213, v1, v223
	v_mul_f32_e32 v1, v205, v237
	v_mul_f32_e32 v205, v1, v213
	v_mul_f32_e32 v1, v141, v234
	v_mul_f32_e32 v141, v1, v205
	v_mul_f32_e32 v1, v132, v233
	v_mul_f32_e32 v132, v1, v141
	v_mul_f32_e32 v1, v123, v83
	v_mul_f32_e32 v1, v1, v132
	v_mul_f32_e32 v76, v198, v1
	s_mov_b32 s0, 0x2081cea
	s_mov_b64 s[72:73], exec
	v_cmp_gt_f32_e64 s[0:1], s0, v76
	s_and_saveexec_b64 s[94:95], s[6:7]
	s_cmp_eq_u64 s[0:1], s[72:73]
	s_cselect_b64 s[0:1], -1, 0
	v_cndmask_b32_e64 v1, 0, 1, s[0:1]
	v_mov_b32_e32 v123, s77
	ds_write_b32 v123, v1 offset:51712
	s_or_b64 exec, exec, s[94:95]
	v_mul_f32_e32 v95, v95, v138
	v_mul_f32_e32 v122, v122, v235
	v_cndmask_b32_e64 v138, 1.0, v243, s[74:75]
	v_mul_f32_e32 v82, v82, v232
	v_cndmask_b32_e64 v122, 0, v122, s[70:71]
	v_mul_f32_e32 v138, v198, v138
	v_mul_f32_e32 v81, v81, v230
	v_cndmask_b32_e64 v82, 0, v82, s[68:69]
	v_mul_f32_e32 v122, v122, v138
	v_mul_f32_e32 v138, v236, v138
	v_mul_f32_e32 v123, v139, v140
	v_mul_f32_e32 v80, v80, v228
	v_cndmask_b32_e64 v81, 0, v81, s[66:67]
	v_mul_f32_e32 v139, v82, v138
	v_mul_f32_e32 v82, v231, v138
	v_cndmask_b32_e64 v80, 0, v80, s[64:65]
	v_mul_f32_e32 v138, v81, v82
	v_mul_f32_e32 v81, v229, v82
	v_mul_f32_e32 v140, v80, v81
	v_mul_f32_e32 v80, v198, v242
	v_cndmask_b32_e64 v81, 1.0, v241, s[74:75]
	v_mul_f32_e32 v80, v81, v80
	v_mul_f32_e32 v86, v86, v120
	v_mul_f32_e32 v87, v87, v121
	v_mul_f32_e32 v120, v134, v135
	v_mul_f32_e32 v121, v136, v137
	v_mul_f32_e32 v135, v221, v222
	v_mul_f32_e32 v136, v224, v225
	v_mul_f32_e32 v79, v79, v80
	v_cndmask_b32_e64 v135, 0, v135, s[58:59]
	v_cndmask_b32_e64 v136, 0, v136, s[60:61]
	v_mul_f32_e32 v78, v78, v79
	v_mul_f32_e32 v136, v136, v79
	v_mul_f32_e32 v82, v135, v78
	v_mul_f32_e32 v77, v77, v78
	v_mul_f32_e32 v78, v198, v240
	v_cndmask_b32_e64 v79, 1.0, v239, s[74:75]
	v_mul_f32_e32 v78, v79, v78
	v_mul_f32_e32 v75, v75, v78
	v_mul_f32_e32 v1, v116, v117
	v_mul_f32_e32 v116, v118, v119
	v_mul_f32_e32 v118, v129, v130
	v_mul_f32_e32 v72, v72, v210
	v_mul_f32_e32 v130, v211, v212
	v_mul_f32_e32 v137, v226, v227
	v_mul_f32_e32 v74, v74, v75
	v_cndmask_b32_e64 v72, 0, v72, s[48:49]
	v_cndmask_b32_e64 v130, 0, v130, s[50:51]
	v_cndmask_b32_e64 v137, 0, v137, s[62:63]
	v_mul_f32_e32 v73, v73, v74
	v_mul_f32_e32 v137, v137, v80
	v_mul_f32_e32 v80, v130, v74
	v_mul_f32_e32 v130, v72, v73
	v_mul_f32_e32 v72, v198, v223
	v_cndmask_b32_e64 v73, 1.0, v238, s[74:75]
	v_mul_f32_e32 v72, v73, v72
	v_mul_f32_e32 v70, v70, v72
	v_mul_f32_e32 v117, v127, v128
	v_mul_f32_e32 v119, v131, v133
	v_mul_f32_e32 v127, v202, v203
	v_mul_f32_e32 v128, v204, v206
	v_mul_f32_e32 v133, v217, v218
	v_mul_f32_e32 v69, v69, v70
	v_cndmask_b32_e64 v127, 0, v127, s[40:41]
	v_cndmask_b32_e64 v128, 0, v128, s[42:43]
	v_cndmask_b32_e64 v133, 0, v133, s[54:55]
	v_mul_f32_e32 v68, v68, v69
	v_mul_f32_e32 v99, v99, v201
	v_mul_f32_e32 v131, v214, v215
	v_mul_f32_e32 v81, v133, v78
	v_mul_f32_e32 v78, v128, v69
	v_mul_f32_e32 v127, v127, v68
	v_mul_f32_e32 v68, v198, v213
	v_cndmask_b32_e64 v69, 1.0, v237, s[74:75]
	v_mul_f32_e32 v89, v89, v126
	v_mul_f32_e32 v126, v199, v200
	v_cndmask_b32_e64 v99, 0, v99, s[38:39]
	v_cndmask_b32_e64 v131, 0, v131, s[52:53]
	v_mul_f32_e32 v68, v69, v68
	v_mul_f32_e32 v88, v88, v124
	v_mul_f32_e32 v124, v142, v143
	v_cndmask_b32_e64 v126, 0, v126, s[36:37]
	v_mul_f32_e32 v131, v131, v75
	v_mul_f32_e32 v75, v99, v68
	v_mul_f32_e32 v68, v98, v68
	v_cndmask_b32_e64 v124, 0, v124, s[34:35]
	v_mul_f32_e32 v98, v126, v68
	v_mul_f32_e32 v68, v97, v68
	v_cndmask_b32_e64 v123, 0, v123, s[30:31]
	v_mul_f32_e32 v74, v124, v68
	v_mul_f32_e32 v68, v96, v68
	v_mul_f32_e32 v96, v123, v68
	v_mul_f32_e32 v68, v198, v205
	v_cndmask_b32_e64 v69, 1.0, v234, s[74:75]
	v_cndmask_b32_e64 v95, 0, v95, s[28:29]
	v_mul_f32_e32 v68, v69, v68
	v_cndmask_b32_e64 v121, 0, v121, s[26:27]
	v_mul_f32_e32 v71, v71, v209
	v_mul_f32_e32 v73, v95, v68
	v_mul_f32_e32 v68, v94, v68
	v_cndmask_b32_e64 v120, 0, v120, s[24:25]
	v_cndmask_b32_e64 v71, 0, v71, s[46:47]
	v_mul_f32_e32 v94, v121, v68
	v_mul_f32_e32 v68, v93, v68
	v_cndmask_b32_e64 v119, 0, v119, s[22:23]
	v_mul_f32_e32 v79, v71, v72
	v_mul_f32_e32 v72, v120, v68
	v_mul_f32_e32 v68, v92, v68
	v_mul_f32_e32 v92, v119, v68
	v_mul_f32_e32 v68, v198, v141
	v_cndmask_b32_e64 v69, 1.0, v233, s[74:75]
	v_cndmask_b32_e64 v118, 0, v118, s[20:21]
	v_mul_f32_e32 v68, v69, v68
	v_cndmask_b32_e64 v117, 0, v117, s[18:19]
	v_mul_f32_e32 v129, v207, v208
	v_mul_f32_e32 v71, v118, v68
	v_mul_f32_e32 v68, v91, v68
	v_cndmask_b32_e64 v89, 0, v89, s[16:17]
	v_cndmask_b32_e64 v129, 0, v129, s[44:45]
	v_mul_f32_e32 v91, v117, v68
	v_mul_f32_e32 v68, v90, v68
	v_cndmask_b32_e64 v88, 0, v88, s[14:15]
	v_mul_f32_e32 v129, v129, v70
	v_mul_f32_e32 v70, v89, v68
	v_mul_f32_e32 v68, v125, v68
	v_mul_f32_e32 v88, v88, v68
	v_mul_f32_e32 v68, v198, v132
	v_cndmask_b32_e64 v69, 1.0, v83, s[74:75]
	v_cndmask_b32_e64 v87, 0, v87, s[12:13]
	v_mul_f32_e32 v68, v69, v68
	v_cndmask_b32_e64 v86, 0, v86, s[10:11]
	v_mul_f32_e32 v69, v87, v68
	v_mul_f32_e32 v68, v85, v68
	v_cndmask_b32_e64 v116, 0, v116, s[8:9]
	v_mul_f32_e32 v134, v219, v220
	v_mul_f32_e32 v83, v86, v68
	v_mul_f32_e32 v68, v84, v68
	v_cndmask_b32_e32 v1, 0, v1, vcc
	v_cndmask_b32_e64 v134, 0, v134, s[56:57]
	v_mul_f32_e32 v84, v116, v68
	v_mul_f32_e32 v2, v2, v68
	v_mul_f32_e32 v77, v134, v77
	v_mul_f32_e32 v1, v1, v2
	v_cvt_pk_bf16_f32 v68, v1, v84
	v_cvt_pk_bf16_f32 v69, v83, v69
	v_cvt_pk_bf16_f32 v70, v88, v70
	v_cvt_pk_bf16_f32 v71, v91, v71
	v_cvt_pk_bf16_f32 v72, v92, v72
	v_cvt_pk_bf16_f32 v73, v94, v73
	v_cvt_pk_bf16_f32 v74, v96, v74
	v_cvt_pk_bf16_f32 v75, v98, v75
	v_cvt_pk_bf16_f32 v78, v127, v78
	v_cvt_pk_bf16_f32 v79, v129, v79
	v_cvt_pk_bf16_f32 v80, v130, v80
	v_cvt_pk_bf16_f32 v81, v131, v81
	v_cvt_pk_bf16_f32 v82, v77, v82
	v_cvt_pk_bf16_f32 v83, v136, v137
	v_cvt_pk_bf16_f32 v84, v140, v138
	v_cvt_pk_bf16_f32 v85, v139, v122
	s_nop 0
	v_permlane32_swap_b32_e32 v68, v70
	v_permlane32_swap_b32_e32 v69, v71
	v_permlane32_swap_b32_e32 v72, v74
	v_permlane32_swap_b32_e32 v73, v75
	v_permlane32_swap_b32_e32 v78, v80
	v_permlane32_swap_b32_e32 v79, v81
	v_permlane32_swap_b32_e32 v82, v84
	v_permlane32_swap_b32_e32 v83, v85
	ds_read_b64_tr_b16 v[86:87], v145 offset:0
	ds_read_b64_tr_b16 v[88:89], v145 offset:0x800
	ds_read_b64_tr_b16 v[90:91], v145 offset:0x1000
	ds_read_b64_tr_b16 v[92:93], v145 offset:0x1800
	ds_read_b64_tr_b16 v[94:95], v145 offset:0x2000
	ds_read_b64_tr_b16 v[96:97], v145 offset:0x2800
	ds_read_b64_tr_b16 v[116:117], v145 offset:0x3000
	ds_read_b64_tr_b16 v[118:119], v145 offset:0x3800
	ds_read_b64_tr_b16 v[120:121], v145 offset:0x200
	ds_read_b64_tr_b16 v[122:123], v145 offset:0xa00
	ds_read_b64_tr_b16 v[124:125], v145 offset:0x1200
	ds_read_b64_tr_b16 v[126:127], v145 offset:0x1a00
	ds_read_b64_tr_b16 v[128:129], v145 offset:0x2200
	ds_read_b64_tr_b16 v[130:131], v145 offset:0x2a00
	ds_read_b64_tr_b16 v[132:133], v145 offset:0x3200
	ds_read_b64_tr_b16 v[134:135], v145 offset:0x3a00
	s_waitcnt lgkmcnt(8)
	s_nop 0
	v_mfma_f32_32x32x16_bf16 v[52:67], v[68:71], v[86:89], v[52:67]
	v_mfma_f32_32x32x16_bf16 v[52:67], v[72:75], v[90:93], v[52:67]
	v_mfma_f32_32x32x16_bf16 v[52:67], v[78:81], v[94:97], v[52:67]
	v_mfma_f32_32x32x16_bf16 v[52:67], v[82:85], v[116:119], v[52:67]
	ds_read_b64_tr_b16 v[86:87], v145 offset:0x400
	ds_read_b64_tr_b16 v[88:89], v145 offset:0xc00
	ds_read_b64_tr_b16 v[90:91], v145 offset:0x1400
	ds_read_b64_tr_b16 v[92:93], v145 offset:0x1c00
	ds_read_b64_tr_b16 v[94:95], v145 offset:0x2400
	ds_read_b64_tr_b16 v[96:97], v145 offset:0x2c00
	ds_read_b64_tr_b16 v[116:117], v145 offset:0x3400
	ds_read_b64_tr_b16 v[118:119], v145 offset:0x3c00
	s_waitcnt lgkmcnt(8)
	v_mfma_f32_32x32x16_bf16 v[36:51], v[68:71], v[120:123], v[36:51]
	v_mfma_f32_32x32x16_bf16 v[36:51], v[72:75], v[124:127], v[36:51]
	v_mfma_f32_32x32x16_bf16 v[36:51], v[78:81], v[128:131], v[36:51]
	v_mfma_f32_32x32x16_bf16 v[36:51], v[82:85], v[132:135], v[36:51]
	ds_read_b64_tr_b16 v[120:121], v145 offset:0x600
	ds_read_b64_tr_b16 v[122:123], v145 offset:0xe00
	ds_read_b64_tr_b16 v[124:125], v145 offset:0x1600
	ds_read_b64_tr_b16 v[126:127], v145 offset:0x1e00
	ds_read_b64_tr_b16 v[128:129], v145 offset:0x2600
	ds_read_b64_tr_b16 v[130:131], v145 offset:0x2e00
	ds_read_b64_tr_b16 v[132:133], v145 offset:0x3600
	ds_read_b64_tr_b16 v[134:135], v145 offset:0x3e00
	s_waitcnt lgkmcnt(8)
	v_mfma_f32_32x32x16_bf16 v[20:35], v[68:71], v[86:89], v[20:35]
	v_mfma_f32_32x32x16_bf16 v[20:35], v[72:75], v[90:93], v[20:35]
	v_mfma_f32_32x32x16_bf16 v[20:35], v[78:81], v[94:97], v[20:35]
	v_mfma_f32_32x32x16_bf16 v[20:35], v[82:85], v[116:119], v[20:35]
	s_waitcnt lgkmcnt(0)
	v_mfma_f32_32x32x16_bf16 v[4:19], v[68:71], v[120:123], v[4:19]
	s_cmp_eq_u32 s88, s2
	v_subrev_u32_e32 v197, 64, v197
	v_subrev_u32_e32 v177, 64, v177
	s_cselect_b64 s[0:1], -1, 0
	v_mfma_f32_32x32x16_bf16 v[4:19], v[72:75], v[124:127], v[4:19]
	v_mfma_f32_32x32x16_bf16 v[4:19], v[78:81], v[128:131], v[4:19]
	v_mfma_f32_32x32x16_bf16 v[4:19], v[82:85], v[132:135], v[4:19]
	s_and_b64 vcc, exec, s[0:1]
	s_cbranch_vccz .LBB0_805
	s_branch .LBB0_786

.LBB0_827:
	v_mov_b64_e32 v[68:69], v[130:131]
	v_lshlrev_b32_e32 v2, 1, v182
	s_waitcnt lgkmcnt(0)
	s_barrier
	v_add_u32_e32 v1, v137, v155
	v_lshl_add_u64 v[214:215], v[68:69], 0, v[2:3]
	global_load_dwordx4 v[84:87], v[214:215], off
	global_load_dwordx4 v[186:189], v[214:215], off offset:32
	global_load_dwordx4 v[190:193], v[214:215], off offset:64
	global_load_dwordx4 v[194:197], v[214:215], off offset:96
	ds_read_b128 v[68:71], v1
	ds_read_b128 v[88:91], v1 offset:16384
	global_load_dwordx4 v[198:201], v[214:215], off offset:128
	v_add_u32_e32 v1, v137, v157
	ds_read_b128 v[202:205], v1
	ds_read_b128 v[206:209], v1 offset:16384
	v_add_u32_e32 v1, v137, v159
	s_waitcnt vmcnt(4) lgkmcnt(3)
	v_mfma_f32_32x32x16_bf16 v[68:83], v[68:71], v[84:87], 0
	s_waitcnt vmcnt(3) lgkmcnt(1)
	v_mfma_f32_32x32x16_bf16 v[68:83], v[202:205], v[186:189], v[68:83]
	global_load_dwordx4 v[202:205], v[214:215], off offset:160
	v_mfma_f32_32x32x16_bf16 v[84:99], v[88:91], v[84:87], 0
	s_waitcnt lgkmcnt(0)
	v_mfma_f32_32x32x16_bf16 v[84:99], v[206:209], v[186:189], v[84:99]
	ds_read_b128 v[186:189], v1
	ds_read_b128 v[206:209], v1 offset:16384
	v_add_u32_e32 v1, v137, v161
	s_waitcnt vmcnt(3) lgkmcnt(1)
	v_mfma_f32_32x32x16_bf16 v[68:83], v[186:189], v[190:193], v[68:83]
	global_load_dwordx4 v[186:189], v[214:215], off offset:192
	s_waitcnt lgkmcnt(0)
	v_mfma_f32_32x32x16_bf16 v[84:99], v[206:209], v[190:193], v[84:99]
	ds_read_b128 v[190:193], v1
	ds_read_b128 v[206:209], v1 offset:16384
	v_add_u32_e32 v1, v137, v163
	s_waitcnt vmcnt(3) lgkmcnt(1)
	v_mfma_f32_32x32x16_bf16 v[68:83], v[190:193], v[194:197], v[68:83]
	global_load_dwordx4 v[190:193], v[214:215], off offset:224
	s_waitcnt lgkmcnt(0)
	v_mfma_f32_32x32x16_bf16 v[84:99], v[206:209], v[194:197], v[84:99]
	ds_read_b128 v[194:197], v1
	ds_read_b128 v[206:209], v1 offset:16384
	v_add_u32_e32 v1, v137, v165
	s_waitcnt vmcnt(3) lgkmcnt(1)
	v_mfma_f32_32x32x16_bf16 v[68:83], v[194:197], v[198:201], v[68:83]
	global_load_dwordx4 v[194:197], v[214:215], off offset:256
	s_waitcnt lgkmcnt(0)
	v_mfma_f32_32x32x16_bf16 v[84:99], v[206:209], v[198:201], v[84:99]
	ds_read_b128 v[198:201], v1
	ds_read_b128 v[206:209], v1 offset:16384
	v_add_u32_e32 v1, v137, v167
	global_load_dwordx4 v[210:213], v[214:215], off offset:320
	s_waitcnt vmcnt(4) lgkmcnt(1)
	v_mfma_f32_32x32x16_bf16 v[68:83], v[198:201], v[202:205], v[68:83]
	global_load_dwordx4 v[198:201], v[214:215], off offset:288
	s_waitcnt lgkmcnt(0)
	v_mfma_f32_32x32x16_bf16 v[84:99], v[206:209], v[202:205], v[84:99]
	ds_read_b128 v[202:205], v1
	ds_read_b128 v[206:209], v1 offset:16384
	global_load_dwordx4 v[218:221], v[214:215], off offset:384
	v_add_u32_e32 v1, v137, v169
	s_waitcnt vmcnt(5) lgkmcnt(1)
	v_mfma_f32_32x32x16_bf16 v[68:83], v[202:205], v[186:189], v[68:83]
	global_load_dwordx4 v[202:205], v[214:215], off offset:352
	s_waitcnt lgkmcnt(0)
	v_mfma_f32_32x32x16_bf16 v[84:99], v[206:209], v[186:189], v[84:99]
	ds_read_b128 v[186:189], v1
	ds_read_b128 v[206:209], v1 offset:16384
	s_waitcnt vmcnt(5) lgkmcnt(1)
	v_mfma_f32_32x32x16_bf16 v[68:83], v[186:189], v[190:193], v[68:83]
	global_load_dwordx4 v[186:189], v[214:215], off offset:416
	global_load_dwordx4 v[222:225], v[214:215], off offset:448
	s_waitcnt lgkmcnt(0)
	v_mfma_f32_32x32x16_bf16 v[84:99], v[206:209], v[190:193], v[84:99]
	ds_read_b128 v[190:193], v142
	ds_read_b128 v[206:209], v142 offset:16384
	s_waitcnt vmcnt(6) lgkmcnt(1)
	v_mfma_f32_32x32x16_bf16 v[68:83], v[190:193], v[194:197], v[68:83]
	global_load_dwordx4 v[190:193], v[214:215], off offset:480
	s_waitcnt lgkmcnt(0)
	v_mfma_f32_32x32x16_bf16 v[84:99], v[206:209], v[194:197], v[84:99]
	ds_read_b128 v[194:197], v143
	ds_read_b128 v[206:209], v143 offset:16384
	s_waitcnt vmcnt(5) lgkmcnt(1)
	v_mfma_f32_32x32x16_bf16 v[68:83], v[194:197], v[198:201], v[68:83]
	ds_read_b128 v[194:197], v171
	ds_read_b128 v[226:229], v171 offset:16384
	s_waitcnt lgkmcnt(1)
	v_mfma_f32_32x32x16_bf16 v[68:83], v[194:197], v[210:213], v[68:83]
	ds_read_b128 v[194:197], v173
	ds_read_b128 v[230:233], v173 offset:16384
	v_mfma_f32_32x32x16_bf16 v[84:99], v[206:209], v[198:201], v[84:99]
	s_waitcnt vmcnt(3) lgkmcnt(1)
	v_mfma_f32_32x32x16_bf16 v[68:83], v[194:197], v[202:205], v[68:83]
	ds_read_b128 v[194:197], v175
	ds_read_b128 v[234:237], v175 offset:16384
	v_mfma_f32_32x32x16_bf16 v[84:99], v[226:229], v[210:213], v[84:99]
	s_waitcnt lgkmcnt(1)
	v_mfma_f32_32x32x16_bf16 v[68:83], v[194:197], v[218:221], v[68:83]
	ds_read_b128 v[194:197], v176
	ds_read_b128 v[238:241], v176 offset:16384
	v_mfma_f32_32x32x16_bf16 v[84:99], v[230:233], v[202:205], v[84:99]
	s_waitcnt vmcnt(2) lgkmcnt(1)
	v_mfma_f32_32x32x16_bf16 v[68:83], v[194:197], v[186:189], v[68:83]
	ds_read_b128 v[194:197], v177
	ds_read_b128 v[242:245], v177 offset:16384
	v_mfma_f32_32x32x16_bf16 v[84:99], v[234:237], v[218:221], v[84:99]
	s_waitcnt vmcnt(1) lgkmcnt(1)
	v_mfma_f32_32x32x16_bf16 v[68:83], v[194:197], v[222:225], v[68:83]
	ds_read_b128 v[194:197], v178
	ds_read_b128 v[246:249], v178 offset:16384
	v_mfma_f32_32x32x16_bf16 v[84:99], v[238:241], v[186:189], v[84:99]
	s_waitcnt vmcnt(0) lgkmcnt(1)
	v_mfma_f32_32x32x16_bf16 v[68:83], v[194:197], v[190:193], v[68:83]
	v_mfma_f32_32x32x16_bf16 v[84:99], v[242:245], v[222:225], v[84:99]
	s_cmp_eq_u32 s14, 0xc6000
	s_cbranch_scc1 .Lmemkv_skip
	v_lshl_add_u64 v[198:199], v[134:135], 0, s[14:15]
	s_mov_b64 s[16:17], 0x3d942000
	v_lshl_add_u64 v[200:201], v[198:199], 0, s[16:17]
	global_load_dwordx4 v[100:103], v[200:201], off
	global_load_dwordx4 v[104:107], v[200:201], off offset:256
	s_mov_b64 s[16:17], 0x3d963000
	v_lshl_add_u64 v[200:201], v[198:199], 0, s[16:17]
	global_load_dwordx4 v[108:111], v[200:201], off
	global_load_dwordx4 v[112:115], v[200:201], off offset:256
	v_lshl_add_u64 v[198:199], v[132:133], 0, s[14:15]
	s_mov_b64 s[16:17], 0x3d942000
	v_lshl_add_u64 v[200:201], v[198:199], 0, s[16:17]
	global_load_dwordx4 v[116:119], v[200:201], off offset:2048
	s_mov_b64 s[16:17], 0x3d963000
	v_lshl_add_u64 v[200:201], v[198:199], 0, s[16:17]
	global_load_dwordx4 v[120:123], v[200:201], off offset:2048
.Lmemkv_skip:
	s_nop 10
	v_max_f32_e32 v1, v69, v69
	v_max_f32_e32 v2, v68, v68
	v_max_f32_e32 v1, v2, v1
	v_max3_f32 v1, v1, v70, v71
	v_max3_f32 v1, v1, v72, v73
	v_max3_f32 v1, v1, v74, v75
	v_max3_f32 v1, v1, v76, v77
	s_waitcnt lgkmcnt(0)
	v_mfma_f32_32x32x16_bf16 v[84:99], v[246:249], v[190:193], v[84:99]
	v_max3_f32 v1, v1, v78, v79
	v_max3_f32 v1, v1, v80, v81
	v_max3_f32 v1, v1, v82, v83
	s_nop 8
	v_max3_f32 v1, v1, v84, v85
	v_max3_f32 v1, v1, v86, v87
	v_max3_f32 v1, v1, v88, v89
	v_max3_f32 v1, v1, v90, v91
	v_max3_f32 v1, v1, v92, v93
	v_max3_f32 v1, v1, v94, v95
	v_max3_f32 v1, v1, v96, v97
	v_max3_f32 v1, v1, v98, v99
	v_mov_b32_e32 v2, v1
	s_nop 1
	v_permlane32_swap_b32_e32 v1, v2
	v_max3_f32 v2, v179, v1, v2
	v_sub_f32_e32 v1, v68, v2
	v_exp_f32_e32 v181, v1
	v_sub_f32_e32 v1, v84, v2
	v_exp_f32_e32 v68, v1
	v_sub_f32_e32 v1, v69, v2
	v_exp_f32_e32 v185, v1
	v_sub_f32_e32 v1, v85, v2
	v_sub_f32_e32 v70, v70, v2
	v_exp_f32_e32 v69, v1
	v_exp_f32_e32 v85, v70
	v_sub_f32_e32 v70, v86, v2
	v_exp_f32_e32 v70, v70
	v_add_f32_e32 v84, v181, v68
	v_sub_f32_e32 v1, v179, v2
	v_add_f32_e32 v84, 0, v84
	v_add_f32_e32 v179, v185, v69
	v_sub_f32_e32 v71, v71, v2
	v_exp_f32_e32 v86, v71
	v_sub_f32_e32 v71, v87, v2
	v_add_f32_e32 v84, v179, v84
	v_add_f32_e32 v87, v85, v70
	v_sub_f32_e32 v72, v72, v2
	v_exp_f32_e32 v71, v71
	v_add_f32_e32 v84, v87, v84
	v_exp_f32_e32 v87, v72
	v_sub_f32_e32 v72, v88, v2
	v_exp_f32_e32 v72, v72
	v_add_f32_e32 v179, v86, v71
	v_sub_f32_e32 v73, v73, v2
	v_exp_f32_e32 v88, v73
	v_sub_f32_e32 v73, v89, v2
	v_add_f32_e32 v84, v179, v84
	v_add_f32_e32 v89, v87, v72
	v_sub_f32_e32 v74, v74, v2
	v_exp_f32_e32 v73, v73
	v_add_f32_e32 v186, v89, v84
	v_exp_f32_e32 v89, v74
	v_sub_f32_e32 v74, v90, v2
	v_exp_f32_e32 v74, v74
	v_sub_f32_e32 v75, v75, v2
	v_add_f32_e32 v187, v88, v73
	v_exp_f32_e32 v179, v75
	v_sub_f32_e32 v75, v91, v2
	v_exp_f32_e32 v84, v75
	v_add_f32_e32 v75, v187, v186
	v_add_f32_e32 v90, v89, v74
	v_add_f32_e32 v186, v90, v75
	v_sub_f32_e32 v75, v76, v2
	v_exp_f32_e32 v90, v75
	v_sub_f32_e32 v75, v92, v2
	v_exp_f32_e32 v75, v75
	v_add_f32_e32 v187, v179, v84
	v_sub_f32_e32 v76, v77, v2
	v_add_f32_e32 v77, v187, v186
	v_add_f32_e32 v92, v90, v75
	v_exp_f32_e32 v91, v76
	v_sub_f32_e32 v76, v93, v2
	v_add_f32_e32 v186, v92, v77
	v_sub_f32_e32 v77, v78, v2
	v_exp_f32_e32 v76, v76
	v_exp_f32_e32 v92, v77
	v_sub_f32_e32 v77, v94, v2
	v_exp_f32_e32 v77, v77
	v_add_f32_e32 v187, v91, v76
	v_sub_f32_e32 v78, v79, v2
	v_add_f32_e32 v79, v187, v186
	v_add_f32_e32 v94, v92, v77
	v_exp_f32_e32 v93, v78
	v_sub_f32_e32 v78, v95, v2
	v_add_f32_e32 v186, v94, v79
	v_sub_f32_e32 v79, v80, v2
	v_exp_f32_e32 v78, v78
	v_exp_f32_e32 v94, v79
	v_sub_f32_e32 v79, v96, v2
	v_exp_f32_e32 v79, v79
	v_add_f32_e32 v187, v93, v78
	v_sub_f32_e32 v80, v81, v2
	v_add_f32_e32 v81, v187, v186
	v_add_f32_e32 v96, v94, v79
	v_exp_f32_e32 v95, v80
	v_sub_f32_e32 v80, v97, v2
	v_add_f32_e32 v186, v96, v81
	v_sub_f32_e32 v81, v82, v2
	v_exp_f32_e32 v80, v80
	v_exp_f32_e32 v96, v81
	v_sub_f32_e32 v81, v98, v2
	v_sub_f32_e32 v82, v83, v2
	v_exp_f32_e32 v81, v81
	v_exp_f32_e32 v97, v82
	v_sub_f32_e32 v82, v99, v2
	v_exp_f32_e32 v82, v82
	v_add_f32_e32 v187, v95, v80
	v_add_f32_e32 v83, v187, v186
	v_add_f32_e32 v98, v96, v81
	v_add_f32_e32 v83, v98, v83
	v_add_f32_e32 v98, v97, v82
	v_add_f32_e32 v83, v98, v83
	v_exp_f32_e32 v98, v1
	v_mov_b32_e32 v99, v83
	s_nop 1
	v_permlane32_swap_b32_e32 v83, v99
	v_cmp_gt_f32_e32 vcc, 1.0, v98
	s_cbranch_vccz .LBB0_831
	s_and_saveexec_b64 s[16:17], s[74:75]
	ds_write_b32 v127, v98 offset:49152
	s_or_b64 exec, exec, s[16:17]
	s_waitcnt lgkmcnt(0)
	v_add_u32_e32 v1, s25, v183
	ds_read_b128 v[186:189], v1 offset:49248
	ds_read_b128 v[190:193], v1 offset:49216
	ds_read_b128 v[194:197], v1 offset:49184
	ds_read_b128 v[198:201], v1 offset:49152
	s_waitcnt lgkmcnt(3)
	v_pk_mul_f32 v[64:65], v[64:65], v[186:187]
	s_waitcnt lgkmcnt(2)
	v_pk_mul_f32 v[60:61], v[60:61], v[190:191]
	s_waitcnt lgkmcnt(1)
	v_pk_mul_f32 v[56:57], v[56:57], v[194:195]
	v_pk_mul_f32 v[66:67], v[66:67], v[188:189]
	v_pk_mul_f32 v[62:63], v[62:63], v[192:193]
	v_pk_mul_f32 v[58:59], v[58:59], v[196:197]
	s_waitcnt lgkmcnt(0)
	v_pk_mul_f32 v[54:55], v[54:55], v[200:201]
	v_pk_mul_f32 v[52:53], v[52:53], v[198:199]
	v_pk_mul_f32 v[48:49], v[48:49], v[186:187]
	v_pk_mul_f32 v[44:45], v[44:45], v[190:191]
	v_pk_mul_f32 v[40:41], v[40:41], v[194:195]
	v_pk_mul_f32 v[50:51], v[50:51], v[188:189]
	v_pk_mul_f32 v[46:47], v[46:47], v[192:193]
	v_pk_mul_f32 v[42:43], v[42:43], v[196:197]
	v_pk_mul_f32 v[38:39], v[38:39], v[200:201]
	v_pk_mul_f32 v[36:37], v[36:37], v[198:199]
	v_pk_mul_f32 v[32:33], v[32:33], v[186:187]
	v_pk_mul_f32 v[28:29], v[28:29], v[190:191]
	v_pk_mul_f32 v[24:25], v[24:25], v[194:195]
	v_pk_mul_f32 v[34:35], v[34:35], v[188:189]
	v_pk_mul_f32 v[30:31], v[30:31], v[192:193]
	v_pk_mul_f32 v[26:27], v[26:27], v[196:197]
	v_pk_mul_f32 v[22:23], v[22:23], v[200:201]
	v_pk_mul_f32 v[20:21], v[20:21], v[198:199]
	v_pk_mul_f32 v[16:17], v[16:17], v[186:187]
	v_pk_mul_f32 v[12:13], v[12:13], v[190:191]
	v_pk_mul_f32 v[8:9], v[8:9], v[194:195]
	v_pk_mul_f32 v[18:19], v[18:19], v[188:189]
	v_pk_mul_f32 v[14:15], v[14:15], v[192:193]
	v_pk_mul_f32 v[10:11], v[10:11], v[196:197]
	v_pk_mul_f32 v[6:7], v[6:7], v[200:201]
	v_pk_mul_f32 v[4:5], v[4:5], v[198:199]
